# one static priority raise for waves 0-3 instead of 4-7 over the attention and HGRN2 phases (comparison of the two halves)
# baseline (speedup 1.0000x reference)
.LBB0_1182:
	s_or_b64 exec, exec, s[6:7]
	v_readfirstlane_b32 s98, v0
	s_nop 3
	s_lshr_b32 s98, s98, 6
	s_cmp_ge_u32 s98, 4
	s_cbranch_scc1 .Lprio_p3
	s_setprio 1
